# speedup vs baseline: 1.0121x; 1.0013x over previous
_Z7k_conv4PKDF16_S0_S0_PKfS2_Pf:
	s_load_dwordx4 s[16:19], s[0:1], 0x20
	s_load_dwordx4 s[20:23], s[0:1], 0x0
	s_mov_b32 s15, 0
	s_cmp_lg_u32 s3, 0
	v_and_b32_e32 v42, 63, v0
	s_waitcnt lgkmcnt(0)
	s_mov_b64 s[12:13], s[18:19]
	v_lshrrev_b32_e32 v1, 5, v0
	v_lshlrev_b32_e32 v43, 4, v0
	s_cbranch_scc0 .LBB2_13
	v_readfirstlane_b32 s3, v0
	s_lshr_b32 s29, s3, 6
	s_lshl_b32 s3, s2, 4
	s_and_b32 s3, s3, 0x70
	s_lshr_b32 s4, s2, 3
	s_add_i32 s3, s3, s4
	s_add_i32 s4, s29, 4
	s_lshl_b32 s6, s3, 1
	s_lshl_b32 s3, s2, 2
	s_mul_hi_u32 s5, s4, 0x24000
	s_mul_i32 s4, s4, 0x24000
	s_add_u32 s4, s22, s4
	s_addc_u32 s5, s23, s5
	v_mov_b32_e32 v41, 0
	v_lshlrev_b32_e32 v40, 4, v42
	v_lshl_add_u64 v[38:39], s[4:5], 0, v[40:41]
	global_load_dwordx4 v[98:101], v40, s[4:5]
	global_load_dwordx4 v[94:97], v40, s[4:5] offset:1024
	global_load_dwordx4 v[90:93], v40, s[4:5] offset:2048
	global_load_dwordx4 v[82:85], v40, s[4:5] offset:3072
	s_movk_i32 s4, 0x1000
	v_add_co_u32_e32 v2, vcc, s4, v38
	s_movk_i32 s4, 0x2000
	s_nop 0
	v_addc_co_u32_e32 v3, vcc, 0, v39, vcc
	v_add_co_u32_e32 v4, vcc, s4, v38
	s_movk_i32 s4, 0x3000
	s_nop 0
	v_addc_co_u32_e32 v5, vcc, 0, v39, vcc
	s_and_b32 s14, s6, 0x7fffffc0
	global_load_dwordx4 v[78:81], v[2:3], off offset:1024
	global_load_dwordx4 v[74:77], v[2:3], off offset:2048
	global_load_dwordx4 v[86:89], v[4:5], off offset:-4096
	global_load_dwordx4 v[66:69], v[4:5], off
	global_load_dwordx4 v[62:65], v[4:5], off offset:1024
	global_load_dwordx4 v[58:61], v[4:5], off offset:2048
	global_load_dwordx4 v[54:57], v[4:5], off offset:3072
	v_add_co_u32_e32 v4, vcc, s4, v38
	s_and_b32 s28, s6, 60
	s_and_b32 s3, s3, 32
	s_lshl_b64 s[4:5], s[14:15], 15
	s_add_u32 s24, s20, s4
	s_addc_u32 s4, s21, s5
	s_add_i32 s10, s3, -1
	v_add_u32_e32 v26, s10, v1
	s_add_i32 s15, s28, 0x1ffff
	v_lshlrev_b32_e32 v27, 9, v26
	v_addc_co_u32_e32 v5, vcc, 0, v39, vcc
	global_load_dwordx4 v[70:73], v[2:3], off offset:3072
	global_load_dwordx4 v[50:53], v[4:5], off
	global_load_dwordx4 v[46:49], v[4:5], off offset:1024
	s_and_b32 s25, s4, 0xffff
	v_and_b32_e32 v41, 0x1f0, v43
	v_lshl_add_u32 v2, s15, 15, v27
	s_movk_i32 s4, 0x33f
	v_or_b32_e32 v2, v2, v41
	v_mov_b32_e32 v44, 0xfffff000
	v_cmp_gt_u32_e32 vcc, 64, v26
	v_not_b32_e32 v18, 33
	v_cmp_lt_u32_e64 s[4:5], s4, v0
	v_cndmask_b32_e32 v10, v44, v2, vcc
	v_mov_b32_e32 v19, s28
	v_cndmask_b32_e64 v2, 0, v18, s[4:5]
	v_add_u32_e32 v2, v1, v2
	v_add3_u32 v2, v2, s10, 8
	v_mov_b32_e32 v20, 0x1ffff
	v_addc_co_u32_e64 v3, s[4:5], v19, v20, s[4:5]
	v_lshlrev_b32_e32 v4, 9, v2
	v_lshl_add_u32 v3, v3, 15, v4
	v_or_b32_e32 v3, v3, v41
	v_cmp_gt_u32_e64 s[4:5], 64, v2
	s_mov_b32 s27, 0x20000
	s_mov_b32 s26, 0x200000
	v_cndmask_b32_e64 v11, v44, v3, s[4:5]
	s_movk_i32 s4, 0x23f
	v_cmp_lt_u32_e64 s[4:5], s4, v0
	v_or_b32_e32 v216, 0xb0, v1
	v_mul_lo_u16_e32 v217, 0xf1, v216
	v_lshrrev_b16_e32 v217, 13, v217
	v_mul_i32_i24_e32 v218, 0xffffffde, v217
	v_add3_u32 v216, s10, v216, v218
	v_add_lshl_u32 v217, s15, v217, 15
	v_cmp_gt_u32_e64 s[30:31], 64, v216
	v_lshl_add_u32 v216, v216, 9, v217
	v_or_b32_e32 v216, v216, v41
	s_movk_i32 s34, 0x380
	v_cmp_gt_u32_e64 s[32:33], s34, v0
	s_nop 1
	s_and_b64 s[30:31], s[32:33], s[30:31]
	v_cndmask_b32_e64 v216, v44, v216, s[30:31]
	buffer_load_dwordx4 v[220:223], v216, s[24:27], 0 offen
	buffer_load_dwordx4 v[2:5], v10, s[24:27], 0 offen
	buffer_load_dwordx4 v[6:9], v11, s[24:27], 0 offen
	v_cndmask_b32_e64 v10, 0, v18, s[4:5]
	v_add_u32_e32 v10, v1, v10
	v_add3_u32 v10, v10, s10, 16
	v_addc_co_u32_e64 v11, s[4:5], v19, v20, s[4:5]
	v_lshlrev_b32_e32 v12, 9, v10
	v_lshl_add_u32 v11, v11, 15, v12
	v_or_b32_e32 v11, v11, v41
	v_cmp_gt_u32_e64 s[4:5], 64, v10
	v_add_u32_e32 v26, 2, v26
	s_lshl_b32 s6, s28, 15
	v_cndmask_b32_e64 v21, v44, v11, s[4:5]
	s_movk_i32 s4, 0x13f
	v_cmp_lt_u32_e64 s[4:5], s4, v0
	v_add_u32_e32 v27, s6, v27
	v_or_b32_e32 v27, v27, v41
	v_cndmask_b32_e64 v10, 0, v18, s[4:5]
	v_add_u32_e32 v10, v1, v10
	v_add3_u32 v10, v10, s10, 24
	v_addc_co_u32_e64 v11, s[4:5], v19, v20, s[4:5]
	v_lshlrev_b32_e32 v12, 9, v10
	v_lshl_add_u32 v11, v11, 15, v12
	v_or_b32_e32 v11, v11, v41
	v_cmp_gt_u32_e64 s[4:5], 64, v10
	v_add_u32_e32 v27, 0x18000, v27
	v_cndmask_b32_e32 v27, v44, v27, vcc
	v_cndmask_b32_e64 v22, v44, v11, s[4:5]
	buffer_load_dwordx4 v[10:13], v21, s[24:27], 0 offen
	buffer_load_dwordx4 v[14:17], v22, s[24:27], 0 offen
	v_or_b32_e32 v21, 32, v1
	v_cmp_lt_u32_e64 s[4:5], 33, v21
	s_movk_i32 s7, 0x80
	s_movk_i32 s11, 0x210
	v_cndmask_b32_e64 v18, 0, v18, s[4:5]
	v_add3_u32 v18, s10, v21, v18
	v_addc_co_u32_e64 v19, s[4:5], v19, v20, s[4:5]
	v_lshlrev_b32_e32 v20, 9, v18
	v_lshl_add_u32 v19, v19, 15, v20
	v_or_b32_e32 v19, v19, v41
	v_cmp_gt_u32_e64 s[4:5], 64, v18
	v_or_b32_e32 v18, 40, v1
	v_mad_u32_u24 v45, v1, s11, v41
	v_cndmask_b32_e64 v28, v44, v19, s[4:5]
	v_mul_lo_u16_e32 v19, 31, v18
	v_lshrrev_b16_e32 v19, 10, v19
	v_mul_i32_i24_e32 v20, 0xffffffde, v19
	v_add3_u32 v18, s10, v18, v20
	v_add_lshl_u32 v19, s15, v19, 15
	v_lshl_add_u32 v19, v18, 9, v19
	v_or_b32_e32 v19, v19, v41
	v_cmp_gt_u32_e64 s[4:5], 64, v18
	s_nop 1
	v_cndmask_b32_e64 v29, v44, v19, s[4:5]
	buffer_load_dwordx4 v[18:21], v28, s[24:27], 0 offen
	buffer_load_dwordx4 v[22:25], v29, s[24:27], 0 offen
	v_or_b32_e32 v28, 48, v1
	v_mul_lo_u16_e32 v29, 31, v28
	v_lshrrev_b16_e32 v29, 10, v29
	v_mul_i32_i24_e32 v30, 0xffffffde, v29
	v_add3_u32 v28, s10, v28, v30
	v_add_lshl_u32 v29, s15, v29, 15
	v_lshl_add_u32 v29, v28, 9, v29
	v_or_b32_e32 v29, v29, v41
	v_cmp_gt_u32_e64 s[4:5], 64, v28
	s_nop 1
	v_cndmask_b32_e64 v28, v44, v29, s[4:5]
	v_or_b32_e32 v29, 56, v1
	v_mul_lo_u16_e32 v30, 31, v29
	v_lshrrev_b16_e32 v30, 10, v30
	v_mul_i32_i24_e32 v31, 0xffffffde, v30
	v_add3_u32 v29, s10, v29, v31
	v_add_lshl_u32 v30, s15, v30, 15
	v_lshl_add_u32 v30, v29, 9, v30
	v_or_b32_e32 v30, v30, v41
	v_cmp_gt_u32_e64 s[4:5], 64, v29
	s_nop 1
	v_cndmask_b32_e64 v29, v44, v30, s[4:5]
	buffer_load_dwordx4 v[102:105], v28, s[24:27], 0 offen
	buffer_load_dwordx4 v[106:109], v29, s[24:27], 0 offen
	v_or_b32_e32 v28, 64, v1
	v_mul_lo_u16_e32 v29, 0x79, v28
	v_lshrrev_b16_e32 v29, 12, v29
	v_mul_i32_i24_e32 v30, 0xffffffde, v29
	v_add3_u32 v28, s10, v28, v30
	v_add_lshl_u32 v29, s15, v29, 15
	v_lshl_add_u32 v29, v28, 9, v29
	v_or_b32_e32 v29, v29, v41
	v_cmp_gt_u32_e64 s[4:5], 64, v28
	s_nop 1
	v_cndmask_b32_e64 v28, v44, v29, s[4:5]
	v_or_b32_e32 v29, 0x48, v1
	v_mul_lo_u16_e32 v30, 0x79, v29
	v_lshrrev_b16_e32 v30, 12, v30
	v_mul_i32_i24_e32 v31, 0xffffffde, v30
	v_add3_u32 v29, s10, v29, v31
	v_add_lshl_u32 v30, s15, v30, 15
	v_lshl_add_u32 v30, v29, 9, v30
	v_or_b32_e32 v30, v30, v41
	v_cmp_gt_u32_e64 s[4:5], 64, v29
	s_nop 1
	v_cndmask_b32_e64 v29, v44, v30, s[4:5]
	buffer_load_dwordx4 v[110:113], v28, s[24:27], 0 offen
	buffer_load_dwordx4 v[114:117], v29, s[24:27], 0 offen
	v_or_b32_e32 v28, 0x50, v1
	v_mul_lo_u16_e32 v29, 0x79, v28
	v_lshrrev_b16_e32 v29, 12, v29
	v_mul_i32_i24_e32 v30, 0xffffffde, v29
	v_add3_u32 v28, s10, v28, v30
	v_add_lshl_u32 v29, s15, v29, 15
	v_lshl_add_u32 v29, v28, 9, v29
	v_or_b32_e32 v29, v29, v41
	v_cmp_gt_u32_e64 s[4:5], 64, v28
	s_nop 1
	v_cndmask_b32_e64 v28, v44, v29, s[4:5]
	v_or_b32_e32 v29, 0x58, v1
	v_mul_lo_u16_e32 v30, 0x79, v29
	v_lshrrev_b16_e32 v30, 12, v30
	v_mul_i32_i24_e32 v31, 0xffffffde, v30
	v_add3_u32 v29, s10, v29, v31
	v_add_lshl_u32 v30, s15, v30, 15
	v_lshl_add_u32 v30, v29, 9, v30
	v_or_b32_e32 v30, v30, v41
	v_cmp_gt_u32_e64 s[4:5], 64, v29
	s_nop 1
	v_cndmask_b32_e64 v29, v44, v30, s[4:5]
	buffer_load_dwordx4 v[118:121], v28, s[24:27], 0 offen
	buffer_load_dwordx4 v[122:125], v29, s[24:27], 0 offen
	v_or_b32_e32 v28, 0x60, v1
	v_mul_lo_u16_e32 v29, 0x79, v28
	v_lshrrev_b16_e32 v29, 12, v29
	v_mul_i32_i24_e32 v30, 0xffffffde, v29
	v_add3_u32 v28, s10, v28, v30
	v_add_lshl_u32 v29, s15, v29, 15
	v_lshl_add_u32 v29, v28, 9, v29
	v_or_b32_e32 v29, v29, v41
	v_cmp_gt_u32_e64 s[4:5], 64, v28
	s_nop 1
	v_cndmask_b32_e64 v28, v44, v29, s[4:5]
	v_lshl_add_u32 v29, v26, 9, s6
	v_or_b32_e32 v29, v29, v41
	v_add_u32_e32 v29, 0x10000, v29
	v_cmp_gt_u32_e64 s[4:5], 64, v26
	s_nop 1
	v_cndmask_b32_e64 v26, v44, v29, s[4:5]
	buffer_load_dwordx4 v[126:129], v28, s[24:27], 0 offen
	buffer_load_dwordx4 v[130:133], v26, s[24:27], 0 offen
	v_or_b32_e32 v26, 0x70, v1
	v_mul_lo_u16_e32 v28, 0x79, v26
	v_lshrrev_b16_e32 v28, 12, v28
	v_mul_i32_i24_e32 v29, 0xffffffde, v28
	v_add3_u32 v26, s10, v26, v29
	v_add_lshl_u32 v28, s15, v28, 15
	v_lshl_add_u32 v28, v26, 9, v28
	v_or_b32_e32 v28, v28, v41
	v_cmp_gt_u32_e64 s[4:5], 64, v26
	s_nop 1
	v_cndmask_b32_e64 v26, v44, v28, s[4:5]
	v_or_b32_e32 v28, 0x78, v1
	v_mul_lo_u16_e32 v29, 0x79, v28
	v_lshrrev_b16_e32 v29, 12, v29
	v_mul_i32_i24_e32 v30, 0xffffffde, v29
	v_add3_u32 v28, s10, v28, v30
	v_add_lshl_u32 v29, s15, v29, 15
	v_lshl_add_u32 v29, v28, 9, v29
	v_or_b32_e32 v29, v29, v41
	v_cmp_gt_u32_e64 s[4:5], 64, v28
	v_or_b32_e32 v30, 0xc8, v1
	v_mul_lo_u16_e32 v31, 0xf1, v30
	v_cndmask_b32_e64 v28, v44, v29, s[4:5]
	buffer_load_dwordx4 v[134:137], v26, s[24:27], 0 offen
	buffer_load_dwordx4 v[138:141], v28, s[24:27], 0 offen
	v_or_b32_e32 v26, 0x80, v1
	v_mul_lo_u16_e32 v28, 0xf1, v26
	v_lshrrev_b16_e32 v28, 13, v28
	v_mul_i32_i24_e32 v29, 0xffffffde, v28
	v_add3_u32 v26, s10, v26, v29
	v_add_lshl_u32 v28, s15, v28, 15
	v_lshl_add_u32 v28, v26, 9, v28
	v_or_b32_e32 v28, v28, v41
	v_cmp_gt_u32_e64 s[4:5], 64, v26
	v_lshrrev_b16_e32 v31, 13, v31
	v_mul_i32_i24_e32 v32, 0xffffffde, v31
	v_cndmask_b32_e64 v26, v44, v28, s[4:5]
	buffer_load_dwordx4 v[142:145], v26, s[24:27], 0 offen
	buffer_load_dwordx4 v[146:149], v27, s[24:27], 0 offen
	v_or_b32_e32 v26, 0x90, v1
	v_mul_lo_u16_e32 v27, 0xf1, v26
	v_lshrrev_b16_e32 v27, 13, v27
	v_mul_i32_i24_e32 v28, 0xffffffde, v27
	v_add3_u32 v26, s10, v26, v28
	v_add_lshl_u32 v27, s15, v27, 15
	v_lshl_add_u32 v27, v26, 9, v27
	v_or_b32_e32 v27, v27, v41
	v_cmp_gt_u32_e32 vcc, 64, v26
	s_movk_i32 s4, 0x280
	v_add3_u32 v30, s10, v30, v32
	v_cndmask_b32_e32 v26, v44, v27, vcc
	v_or_b32_e32 v27, 0x98, v1
	v_mul_lo_u16_e32 v28, 0xf1, v27
	v_lshrrev_b16_e32 v28, 13, v28
	v_mul_i32_i24_e32 v29, 0xffffffde, v28
	v_add3_u32 v27, s10, v27, v29
	v_add_lshl_u32 v28, s15, v28, 15
	v_lshl_add_u32 v28, v27, 9, v28
	v_or_b32_e32 v28, v28, v41
	v_cmp_gt_u32_e32 vcc, 64, v27
	v_add_lshl_u32 v31, s15, v31, 15
	s_nop 0
	v_cndmask_b32_e32 v27, v44, v28, vcc
	buffer_load_dwordx4 v[150:153], v26, s[24:27], 0 offen
	buffer_load_dwordx4 v[154:157], v27, s[24:27], 0 offen
	v_or_b32_e32 v26, 0xa0, v1
	v_mul_lo_u16_e32 v27, 0xf1, v26
	v_lshrrev_b16_e32 v27, 13, v27
	v_mul_i32_i24_e32 v28, 0xffffffde, v27
	v_add3_u32 v26, s10, v26, v28
	v_add_lshl_u32 v27, s15, v27, 15
	v_lshl_add_u32 v27, v26, 9, v27
	v_or_b32_e32 v27, v27, v41
	v_cmp_gt_u32_e32 vcc, 64, v26
	s_nop 1
	v_cndmask_b32_e32 v26, v44, v27, vcc
	v_or_b32_e32 v27, 0xa8, v1
	v_mul_lo_u16_e32 v28, 0xf1, v27
	v_lshrrev_b16_e32 v28, 13, v28
	v_mul_i32_i24_e32 v29, 0xffffffde, v28
	v_add3_u32 v27, s10, v27, v29
	v_add_lshl_u32 v28, s15, v28, 15
	v_lshl_add_u32 v28, v27, 9, v28
	v_or_b32_e32 v28, v28, v41
	v_cmp_gt_u32_e32 vcc, 64, v27
	s_nop 1
	v_cndmask_b32_e32 v27, v44, v28, vcc
	buffer_load_dwordx4 v[158:161], v26, s[24:27], 0 offen
	buffer_load_dwordx4 v[162:165], v27, s[24:27], 0 offen
	v_or_b32_e32 v26, 0xb8, v1
	v_mul_lo_u16_e32 v27, 0xf1, v26
	v_lshrrev_b16_e32 v27, 13, v27
	v_mul_i32_i24_e32 v28, 0xffffffde, v27
	v_add3_u32 v26, s10, v26, v28
	v_add_lshl_u32 v27, s15, v27, 15
	v_cmp_gt_u32_e32 vcc, s4, v0
	v_cmp_gt_u32_e64 s[4:5], 64, v26
	v_lshl_add_u32 v26, v26, 9, v27
	v_or_b32_e32 v27, 0xc0, v1
	v_mul_lo_u16_e32 v28, 0xf1, v27
	v_or_b32_e32 v26, v26, v41
	s_and_b64 s[4:5], vcc, s[4:5]
	v_lshrrev_b16_e32 v28, 13, v28
	v_cndmask_b32_e64 v26, v44, v26, s[4:5]
	v_mul_i32_i24_e32 v29, 0xffffffde, v28
	s_movk_i32 s4, 0xcc
	v_add3_u32 v29, s10, v27, v29
	v_cmp_gt_u32_e64 s[8:9], s4, v27
	v_add_lshl_u32 v27, s15, v28, 15
	v_cmp_gt_u32_e64 s[4:5], 64, v29
	v_lshl_add_u32 v27, v29, 9, v27
	v_or_b32_e32 v27, v27, v41
	s_and_b64 s[4:5], s[8:9], s[4:5]
	v_cndmask_b32_e64 v27, v44, v27, s[4:5]
	v_cmp_gt_u32_e64 s[4:5], s7, v0
	v_cmp_gt_u32_e64 s[6:7], 64, v30
	v_lshl_add_u32 v30, v30, 9, v31
	v_or_b32_e32 v30, v30, v41
	s_and_b64 s[6:7], s[4:5], s[6:7]
	v_cndmask_b32_e64 v30, v44, v30, s[6:7]
	buffer_load_dwordx4 v[34:37], v26, s[24:27], 0 offen
	s_nop 0
	buffer_load_dwordx4 v[26:29], v27, s[24:27], 0 offen
	s_movk_i32 s6, 0x380
	buffer_load_dwordx4 v[30:33], v30, s[24:27], 0 offen
	s_waitcnt vmcnt(24)
	ds_write_b128 v45, v[2:5]
	s_waitcnt vmcnt(23)
	ds_write_b128 v45, v[6:9] offset:4224
	s_waitcnt vmcnt(22)
	ds_write_b128 v45, v[10:13] offset:8448
	s_waitcnt vmcnt(21)
	ds_write_b128 v45, v[14:17] offset:12672
	s_waitcnt vmcnt(20)
	ds_write_b128 v45, v[18:21] offset:16896
	s_waitcnt vmcnt(19)
	ds_write_b128 v45, v[22:25] offset:21120
	s_waitcnt vmcnt(18)
	ds_write_b128 v45, v[102:105] offset:25344
	s_waitcnt vmcnt(17)
	ds_write_b128 v45, v[106:109] offset:29568
	s_waitcnt vmcnt(16)
	ds_write_b128 v45, v[110:113] offset:33792
	s_waitcnt vmcnt(15)
	ds_write_b128 v45, v[114:117] offset:38016
	s_waitcnt vmcnt(14)
	ds_write_b128 v45, v[118:121] offset:42240
	s_waitcnt vmcnt(13)
	ds_write_b128 v45, v[122:125] offset:46464
	s_waitcnt vmcnt(12)
	ds_write_b128 v45, v[126:129] offset:50688
	s_waitcnt vmcnt(11)
	ds_write_b128 v45, v[130:133] offset:54912
	s_waitcnt vmcnt(10)
	ds_write_b128 v45, v[134:137] offset:59136
	v_mov_b32_e32 v2, 0xf780
	v_mad_u32_u24 v2, v1, s11, v2
	v_cmp_gt_u32_e64 s[6:7], s6, v0
	v_add_u32_e32 v2, v41, v2
	v_add_u32_e32 v3, 0x11880, v45
	s_waitcnt vmcnt(9)
	ds_write_b128 v2, v[138:141]
	s_waitcnt vmcnt(8)
	ds_write_b128 v2, v[142:145] offset:4224
	s_waitcnt vmcnt(7)
	ds_write_b128 v3, v[146:149]
	s_waitcnt vmcnt(6)
	ds_write_b128 v2, v[150:153] offset:12672
	s_waitcnt vmcnt(5)
	ds_write_b128 v2, v[154:157] offset:16896
	s_waitcnt vmcnt(4)
	ds_write_b128 v2, v[158:161] offset:21120
	s_waitcnt vmcnt(3)
	ds_write_b128 v2, v[162:165] offset:25344
	s_and_saveexec_b64 s[18:19], s[6:7]
	s_cbranch_execz .LBB2_5
	s_waitcnt vmcnt(0)
	ds_write_b128 v2, v[220:223] offset:29568
	s_or_b64 exec, exec, s[18:19]
	s_and_saveexec_b64 s[6:7], vcc
	s_cbranch_execnz .LBB2_6

.LBB2_13:
	s_cbranch_execz .LBB2_12
	v_readfirstlane_b32 s3, v0
	s_lshr_b32 s26, s3, 6
	s_lshl_b32 s3, s2, 4
	s_and_b32 s3, s3, 0x70
	s_lshr_b32 s4, s2, 3
	s_add_i32 s3, s3, s4
	s_lshl_b32 s4, s3, 1
	s_lshl_b32 s2, s2, 2
	s_mul_i32 s6, s26, 0x24000
	s_mul_hi_u32 s5, s26, 0x24000
	s_add_u32 s18, s22, s6
	s_load_dwordx2 s[14:15], s[0:1], 0x10
	s_addc_u32 s19, s23, s5
	v_mov_b32_e32 v35, 0
	v_lshlrev_b32_e32 v34, 4, v42
	v_lshl_add_u64 v[32:33], s[18:19], 0, v[34:35]
	s_movk_i32 s5, 0x1000
	v_add_co_u32_e32 v2, vcc, s5, v32
	s_movk_i32 s6, 0x2000
	s_nop 0
	v_addc_co_u32_e32 v3, vcc, 0, v33, vcc
	s_mov_b32 s11, 0
	v_add_co_u32_e32 v4, vcc, s6, v32
	s_lshr_b32 s10, s3, 5
	s_waitcnt lgkmcnt(0)
	v_lshl_add_u64 v[30:31], s[14:15], 0, v[34:35]
	v_addc_co_u32_e32 v5, vcc, 0, v33, vcc
	s_and_b32 s27, s4, 60
	s_and_b32 s28, s2, 32
	s_lshl_b64 s[2:3], s[10:11], 21
	global_load_dwordx4 v[126:129], v34, s[18:19]
	global_load_dwordx4 v[118:121], v34, s[18:19] offset:1024
	global_load_dwordx4 v[114:117], v34, s[18:19] offset:2048
	global_load_dwordx4 v[106:109], v34, s[18:19] offset:3072
	global_load_dwordx4 v[122:125], v34, s[14:15]
	global_load_dwordx4 v[102:105], v34, s[14:15] offset:1024
	global_load_dwordx4 v[94:97], v[2:3], off offset:1024
	global_load_dwordx4 v[90:93], v[2:3], off offset:2048
	global_load_dwordx4 v[86:89], v[2:3], off offset:3072
	global_load_dwordx4 v[98:101], v34, s[14:15] offset:2048
	global_load_dwordx4 v[82:85], v34, s[14:15] offset:3072
	global_load_dwordx4 v[110:113], v[4:5], off offset:-4096
	global_load_dwordx4 v[78:81], v[4:5], off
	v_add_co_u32_e32 v2, vcc, s5, v30
	s_add_u32 s20, s20, s2
	s_nop 0
	v_addc_co_u32_e32 v3, vcc, 0, v31, vcc
	s_movk_i32 s5, 0x3000
	s_addc_u32 s2, s21, s3
	s_add_i32 s8, s28, -1
	global_load_dwordx4 v[70:73], v[4:5], off offset:1024
	global_load_dwordx4 v[66:69], v[4:5], off offset:2048
	global_load_dwordx4 v[62:65], v[4:5], off offset:3072
	global_load_dwordx4 v[74:77], v[2:3], off
	global_load_dwordx4 v[58:61], v[2:3], off offset:1024
	v_add_co_u32_e32 v4, vcc, s5, v32
	v_add_u32_e32 v18, s8, v1
	s_nop 0
	v_addc_co_u32_e32 v5, vcc, 0, v33, vcc
	s_add_i32 s11, s27, 0x1ffff
	v_lshlrev_b32_e32 v19, 9, v18
	global_load_dwordx4 v[54:57], v[4:5], off
	global_load_dwordx4 v[50:53], v[4:5], off offset:1024
	global_load_dwordx4 v[46:49], v[2:3], off offset:2048
	s_and_b32 s21, s2, 0xffff
	v_and_b32_e32 v35, 0x1f0, v43
	v_lshl_add_u32 v2, s11, 15, v19
	s_movk_i32 s2, 0x33f
	v_or_b32_e32 v2, v2, v35
	v_mov_b32_e32 v36, 0xfffff000
	v_cmp_gt_u32_e32 vcc, 64, v18
	v_not_b32_e32 v20, 33
	v_cmp_lt_u32_e64 s[2:3], s2, v0
	v_cndmask_b32_e32 v10, v36, v2, vcc
	v_mov_b32_e32 v21, s27
	v_cndmask_b32_e64 v2, 0, v20, s[2:3]
	v_add_u32_e32 v2, v1, v2
	v_add3_u32 v2, v2, s8, 8
	v_mov_b32_e32 v22, 0x1ffff
	v_addc_co_u32_e64 v3, s[2:3], v21, v22, s[2:3]
	v_lshlrev_b32_e32 v4, 9, v2
	v_lshl_add_u32 v3, v3, 15, v4
	v_or_b32_e32 v3, v3, v35
	v_cmp_gt_u32_e64 s[2:3], 64, v2
	s_mov_b32 s23, 0x20000
	s_mov_b32 s22, 0x200000
	v_cndmask_b32_e64 v11, v36, v3, s[2:3]
	s_movk_i32 s2, 0x23f
	v_cmp_lt_u32_e64 s[2:3], s2, v0
	v_or_b32_e32 v216, 0xb0, v1
	v_mul_lo_u16_e32 v217, 0xf1, v216
	v_lshrrev_b16_e32 v217, 13, v217
	v_mul_i32_i24_e32 v218, 0xffffffde, v217
	v_add3_u32 v216, s8, v216, v218
	v_add_lshl_u32 v217, s11, v217, 15
	v_cmp_gt_u32_e64 s[30:31], 64, v216
	v_lshl_add_u32 v216, v216, 9, v217
	v_or_b32_e32 v216, v216, v35
	s_movk_i32 s34, 0x380
	v_cmp_gt_u32_e64 s[32:33], s34, v0
	s_nop 1
	s_and_b64 s[30:31], s[32:33], s[30:31]
	v_cndmask_b32_e64 v216, v36, v216, s[30:31]
	buffer_load_dwordx4 v[220:223], v216, s[20:23], 0 offen
	buffer_load_dwordx4 v[2:5], v10, s[20:23], 0 offen
	buffer_load_dwordx4 v[6:9], v11, s[20:23], 0 offen
	v_cndmask_b32_e64 v10, 0, v20, s[2:3]
	v_add_u32_e32 v10, v1, v10
	v_add3_u32 v10, v10, s8, 16
	v_addc_co_u32_e64 v11, s[2:3], v21, v22, s[2:3]
	v_lshlrev_b32_e32 v12, 9, v10
	v_lshl_add_u32 v11, v11, 15, v12
	v_or_b32_e32 v11, v11, v35
	v_cmp_gt_u32_e64 s[2:3], 64, v10
	v_add_u32_e32 v18, 2, v18
	s_lshl_b32 s4, s27, 15
	v_cndmask_b32_e64 v23, v36, v11, s[2:3]
	s_movk_i32 s2, 0x13f
	v_cmp_lt_u32_e64 s[2:3], s2, v0
	v_add_u32_e32 v19, s4, v19
	v_or_b32_e32 v19, v19, v35
	v_cndmask_b32_e64 v10, 0, v20, s[2:3]
	v_add_u32_e32 v10, v1, v10
	v_add3_u32 v10, v10, s8, 24
	v_addc_co_u32_e64 v11, s[2:3], v21, v22, s[2:3]
	v_lshlrev_b32_e32 v12, 9, v10
	v_lshl_add_u32 v11, v11, 15, v12
	v_or_b32_e32 v11, v11, v35
	v_cmp_gt_u32_e64 s[2:3], 64, v10
	v_add_u32_e32 v19, 0x18000, v19
	v_cndmask_b32_e32 v19, v36, v19, vcc
	v_cndmask_b32_e64 v24, v36, v11, s[2:3]
	buffer_load_dwordx4 v[10:13], v23, s[20:23], 0 offen
	buffer_load_dwordx4 v[14:17], v24, s[20:23], 0 offen
	v_or_b32_e32 v23, 32, v1
	v_cmp_lt_u32_e64 s[2:3], 33, v23
	s_movk_i32 s6, 0x80
	s_movk_i32 s9, 0x210
	v_cndmask_b32_e64 v20, 0, v20, s[2:3]
	v_add3_u32 v20, s8, v23, v20
	v_addc_co_u32_e64 v21, s[2:3], v21, v22, s[2:3]
	v_lshlrev_b32_e32 v22, 9, v20
	v_lshl_add_u32 v21, v21, 15, v22
	v_or_b32_e32 v21, v21, v35
	v_cmp_gt_u32_e64 s[2:3], 64, v20
	v_mad_u32_u24 v37, v1, s9, v35
	s_nop 0
	v_cndmask_b32_e64 v20, v36, v21, s[2:3]
	v_or_b32_e32 v21, 40, v1
	v_mul_lo_u16_e32 v22, 31, v21
	v_lshrrev_b16_e32 v22, 10, v22
	v_mul_i32_i24_e32 v23, 0xffffffde, v22
	v_add3_u32 v21, s8, v21, v23
	v_add_lshl_u32 v22, s11, v22, 15
	v_lshl_add_u32 v22, v21, 9, v22
	v_or_b32_e32 v22, v22, v35
	v_cmp_gt_u32_e64 s[2:3], 64, v21
	s_nop 1
	v_cndmask_b32_e64 v21, v36, v22, s[2:3]
	buffer_load_dwordx4 v[38:41], v20, s[20:23], 0 offen
	buffer_load_dwordx4 v[130:133], v21, s[20:23], 0 offen
	v_or_b32_e32 v20, 48, v1
	v_mul_lo_u16_e32 v21, 31, v20
	v_lshrrev_b16_e32 v21, 10, v21
	v_mul_i32_i24_e32 v22, 0xffffffde, v21
	v_add3_u32 v20, s8, v20, v22
	v_add_lshl_u32 v21, s11, v21, 15
	v_lshl_add_u32 v21, v20, 9, v21
	v_or_b32_e32 v21, v21, v35
	v_cmp_gt_u32_e64 s[2:3], 64, v20
	s_nop 1
	v_cndmask_b32_e64 v20, v36, v21, s[2:3]
	v_or_b32_e32 v21, 56, v1
	v_mul_lo_u16_e32 v22, 31, v21
	v_lshrrev_b16_e32 v22, 10, v22
	v_mul_i32_i24_e32 v23, 0xffffffde, v22
	v_add3_u32 v21, s8, v21, v23
	v_add_lshl_u32 v22, s11, v22, 15
	v_lshl_add_u32 v22, v21, 9, v22
	v_or_b32_e32 v22, v22, v35
	v_cmp_gt_u32_e64 s[2:3], 64, v21
	s_nop 1
	v_cndmask_b32_e64 v21, v36, v22, s[2:3]
	buffer_load_dwordx4 v[134:137], v20, s[20:23], 0 offen
	buffer_load_dwordx4 v[138:141], v21, s[20:23], 0 offen
	v_or_b32_e32 v20, 64, v1
	v_mul_lo_u16_e32 v21, 0x79, v20
	v_lshrrev_b16_e32 v21, 12, v21
	v_mul_i32_i24_e32 v22, 0xffffffde, v21
	v_add3_u32 v20, s8, v20, v22
	v_add_lshl_u32 v21, s11, v21, 15
	v_lshl_add_u32 v21, v20, 9, v21
	v_or_b32_e32 v21, v21, v35
	v_cmp_gt_u32_e64 s[2:3], 64, v20
	s_nop 1
	v_cndmask_b32_e64 v20, v36, v21, s[2:3]
	v_or_b32_e32 v21, 0x48, v1
	v_mul_lo_u16_e32 v22, 0x79, v21
	v_lshrrev_b16_e32 v22, 12, v22
	v_mul_i32_i24_e32 v23, 0xffffffde, v22
	v_add3_u32 v21, s8, v21, v23
	v_add_lshl_u32 v22, s11, v22, 15
	v_lshl_add_u32 v22, v21, 9, v22
	v_or_b32_e32 v22, v22, v35
	v_cmp_gt_u32_e64 s[2:3], 64, v21
	s_nop 1
	v_cndmask_b32_e64 v21, v36, v22, s[2:3]
	buffer_load_dwordx4 v[142:145], v20, s[20:23], 0 offen
	buffer_load_dwordx4 v[146:149], v21, s[20:23], 0 offen
	v_or_b32_e32 v20, 0x50, v1
	v_mul_lo_u16_e32 v21, 0x79, v20
	v_lshrrev_b16_e32 v21, 12, v21
	v_mul_i32_i24_e32 v22, 0xffffffde, v21
	v_add3_u32 v20, s8, v20, v22
	v_add_lshl_u32 v21, s11, v21, 15
	v_lshl_add_u32 v21, v20, 9, v21
	v_or_b32_e32 v21, v21, v35
	v_cmp_gt_u32_e64 s[2:3], 64, v20
	s_nop 1
	v_cndmask_b32_e64 v20, v36, v21, s[2:3]
	v_or_b32_e32 v21, 0x58, v1
	v_mul_lo_u16_e32 v22, 0x79, v21
	v_lshrrev_b16_e32 v22, 12, v22
	v_mul_i32_i24_e32 v23, 0xffffffde, v22
	v_add3_u32 v21, s8, v21, v23
	v_add_lshl_u32 v22, s11, v22, 15
	v_lshl_add_u32 v22, v21, 9, v22
	v_or_b32_e32 v22, v22, v35
	v_cmp_gt_u32_e64 s[2:3], 64, v21
	s_nop 1
	v_cndmask_b32_e64 v21, v36, v22, s[2:3]
	buffer_load_dwordx4 v[150:153], v20, s[20:23], 0 offen
	buffer_load_dwordx4 v[154:157], v21, s[20:23], 0 offen
	v_or_b32_e32 v20, 0x60, v1
	v_mul_lo_u16_e32 v21, 0x79, v20
	v_lshrrev_b16_e32 v21, 12, v21
	v_mul_i32_i24_e32 v22, 0xffffffde, v21
	v_add3_u32 v20, s8, v20, v22
	v_add_lshl_u32 v21, s11, v21, 15
	v_lshl_add_u32 v21, v20, 9, v21
	v_or_b32_e32 v21, v21, v35
	v_cmp_gt_u32_e64 s[2:3], 64, v20
	s_nop 1
	v_cndmask_b32_e64 v20, v36, v21, s[2:3]
	v_lshl_add_u32 v21, v18, 9, s4
	v_or_b32_e32 v21, v21, v35
	v_add_u32_e32 v21, 0x10000, v21
	v_cmp_gt_u32_e64 s[2:3], 64, v18
	s_nop 1
	v_cndmask_b32_e64 v18, v36, v21, s[2:3]
	buffer_load_dwordx4 v[158:161], v20, s[20:23], 0 offen
	buffer_load_dwordx4 v[162:165], v18, s[20:23], 0 offen
	v_or_b32_e32 v18, 0x70, v1
	v_mul_lo_u16_e32 v20, 0x79, v18
	v_lshrrev_b16_e32 v20, 12, v20
	v_mul_i32_i24_e32 v21, 0xffffffde, v20
	v_add3_u32 v18, s8, v18, v21
	v_add_lshl_u32 v20, s11, v20, 15
	v_lshl_add_u32 v20, v18, 9, v20
	v_or_b32_e32 v20, v20, v35
	v_cmp_gt_u32_e64 s[2:3], 64, v18
	s_nop 1
	v_cndmask_b32_e64 v18, v36, v20, s[2:3]
	v_or_b32_e32 v20, 0x78, v1
	v_mul_lo_u16_e32 v21, 0x79, v20
	v_lshrrev_b16_e32 v21, 12, v21
	v_mul_i32_i24_e32 v22, 0xffffffde, v21
	v_add3_u32 v20, s8, v20, v22
	v_add_lshl_u32 v21, s11, v21, 15
	v_lshl_add_u32 v21, v20, 9, v21
	v_or_b32_e32 v21, v21, v35
	v_cmp_gt_u32_e64 s[2:3], 64, v20
	v_or_b32_e32 v22, 0xc8, v1
	v_mul_lo_u16_e32 v23, 0xf1, v22
	v_cndmask_b32_e64 v20, v36, v21, s[2:3]
	buffer_load_dwordx4 v[166:169], v18, s[20:23], 0 offen
	buffer_load_dwordx4 v[170:173], v20, s[20:23], 0 offen
	v_or_b32_e32 v18, 0x80, v1
	v_mul_lo_u16_e32 v20, 0xf1, v18
	v_lshrrev_b16_e32 v20, 13, v20
	v_mul_i32_i24_e32 v21, 0xffffffde, v20
	v_add3_u32 v18, s8, v18, v21
	v_add_lshl_u32 v20, s11, v20, 15
	v_lshl_add_u32 v20, v18, 9, v20
	v_or_b32_e32 v20, v20, v35
	v_cmp_gt_u32_e64 s[2:3], 64, v18
	v_lshrrev_b16_e32 v23, 13, v23
	v_mul_i32_i24_e32 v24, 0xffffffde, v23
	v_cndmask_b32_e64 v18, v36, v20, s[2:3]
	buffer_load_dwordx4 v[174:177], v18, s[20:23], 0 offen
	buffer_load_dwordx4 v[178:181], v19, s[20:23], 0 offen
	v_or_b32_e32 v18, 0x90, v1
	v_mul_lo_u16_e32 v19, 0xf1, v18
	v_lshrrev_b16_e32 v19, 13, v19
	v_mul_i32_i24_e32 v20, 0xffffffde, v19
	v_add3_u32 v18, s8, v18, v20
	v_add_lshl_u32 v19, s11, v19, 15
	v_lshl_add_u32 v19, v18, 9, v19
	v_or_b32_e32 v19, v19, v35
	v_cmp_gt_u32_e32 vcc, 64, v18
	s_movk_i32 s2, 0x280
	v_add3_u32 v22, s8, v22, v24
	v_cndmask_b32_e32 v18, v36, v19, vcc
	v_or_b32_e32 v19, 0x98, v1
	v_mul_lo_u16_e32 v20, 0xf1, v19
	v_lshrrev_b16_e32 v20, 13, v20
	v_mul_i32_i24_e32 v21, 0xffffffde, v20
	v_add3_u32 v19, s8, v19, v21
	v_add_lshl_u32 v20, s11, v20, 15
	v_lshl_add_u32 v20, v19, 9, v20
	v_or_b32_e32 v20, v20, v35
	v_cmp_gt_u32_e32 vcc, 64, v19
	v_add_lshl_u32 v23, s11, v23, 15
	s_nop 0
	v_cndmask_b32_e32 v19, v36, v20, vcc
	buffer_load_dwordx4 v[182:185], v18, s[20:23], 0 offen
	buffer_load_dwordx4 v[186:189], v19, s[20:23], 0 offen
	v_or_b32_e32 v18, 0xa0, v1
	v_mul_lo_u16_e32 v19, 0xf1, v18
	v_lshrrev_b16_e32 v19, 13, v19
	v_mul_i32_i24_e32 v20, 0xffffffde, v19
	v_add3_u32 v18, s8, v18, v20
	v_add_lshl_u32 v19, s11, v19, 15
	v_lshl_add_u32 v19, v18, 9, v19
	v_or_b32_e32 v19, v19, v35
	v_cmp_gt_u32_e32 vcc, 64, v18
	s_nop 1
	v_cndmask_b32_e32 v18, v36, v19, vcc
	v_or_b32_e32 v19, 0xa8, v1
	v_mul_lo_u16_e32 v20, 0xf1, v19
	v_lshrrev_b16_e32 v20, 13, v20
	v_mul_i32_i24_e32 v21, 0xffffffde, v20
	v_add3_u32 v19, s8, v19, v21
	v_add_lshl_u32 v20, s11, v20, 15
	v_lshl_add_u32 v20, v19, 9, v20
	v_or_b32_e32 v20, v20, v35
	v_cmp_gt_u32_e32 vcc, 64, v19
	s_nop 1
	v_cndmask_b32_e32 v19, v36, v20, vcc
	buffer_load_dwordx4 v[190:193], v18, s[20:23], 0 offen
	buffer_load_dwordx4 v[194:197], v19, s[20:23], 0 offen
	v_or_b32_e32 v18, 0xb8, v1
	v_mul_lo_u16_e32 v19, 0xf1, v18
	v_lshrrev_b16_e32 v19, 13, v19
	v_mul_i32_i24_e32 v20, 0xffffffde, v19
	v_add3_u32 v18, s8, v18, v20
	v_add_lshl_u32 v19, s11, v19, 15
	v_cmp_gt_u32_e32 vcc, s2, v0
	v_cmp_gt_u32_e64 s[2:3], 64, v18
	v_lshl_add_u32 v18, v18, 9, v19
	v_or_b32_e32 v19, 0xc0, v1
	v_mul_lo_u16_e32 v20, 0xf1, v19
	v_or_b32_e32 v18, v18, v35
	s_and_b64 s[2:3], vcc, s[2:3]
	v_lshrrev_b16_e32 v20, 13, v20
	v_cndmask_b32_e64 v18, v36, v18, s[2:3]
	v_mul_i32_i24_e32 v21, 0xffffffde, v20
	s_movk_i32 s2, 0xcc
	v_add3_u32 v21, s8, v19, v21
	v_cmp_gt_u32_e64 s[2:3], s2, v19
	v_add_lshl_u32 v19, s11, v20, 15
	v_cmp_gt_u32_e64 s[4:5], 64, v21
	v_lshl_add_u32 v19, v21, 9, v19
	v_or_b32_e32 v19, v19, v35
	s_and_b64 s[4:5], s[2:3], s[4:5]
	v_cndmask_b32_e64 v19, v36, v19, s[4:5]
	v_cmp_gt_u32_e64 s[4:5], s6, v0
	v_cmp_gt_u32_e64 s[6:7], 64, v22
	v_lshl_add_u32 v22, v22, 9, v23
	v_or_b32_e32 v22, v22, v35
	s_and_b64 s[6:7], s[4:5], s[6:7]
	v_cndmask_b32_e64 v22, v36, v22, s[6:7]
	buffer_load_dwordx4 v[26:29], v18, s[20:23], 0 offen
	s_nop 0
	buffer_load_dwordx4 v[18:21], v19, s[20:23], 0 offen
	s_movk_i32 s6, 0x380
	buffer_load_dwordx4 v[22:25], v22, s[20:23], 0 offen
	s_waitcnt vmcnt(24)
	ds_write_b128 v37, v[2:5]
	s_waitcnt vmcnt(23)
	ds_write_b128 v37, v[6:9] offset:4224
	s_waitcnt vmcnt(22)
	ds_write_b128 v37, v[10:13] offset:8448
	s_waitcnt vmcnt(21)
	ds_write_b128 v37, v[14:17] offset:12672
	s_waitcnt vmcnt(20)
	ds_write_b128 v37, v[38:41] offset:16896
	s_waitcnt vmcnt(19)
	ds_write_b128 v37, v[130:133] offset:21120
	s_waitcnt vmcnt(18)
	ds_write_b128 v37, v[134:137] offset:25344
	s_waitcnt vmcnt(17)
	ds_write_b128 v37, v[138:141] offset:29568
	s_waitcnt vmcnt(16)
	ds_write_b128 v37, v[142:145] offset:33792
	s_waitcnt vmcnt(15)
	ds_write_b128 v37, v[146:149] offset:38016
	s_waitcnt vmcnt(14)
	ds_write_b128 v37, v[150:153] offset:42240
	s_waitcnt vmcnt(13)
	ds_write_b128 v37, v[154:157] offset:46464
	s_waitcnt vmcnt(12)
	ds_write_b128 v37, v[158:161] offset:50688
	s_waitcnt vmcnt(11)
	ds_write_b128 v37, v[162:165] offset:54912
	s_waitcnt vmcnt(10)
	ds_write_b128 v37, v[166:169] offset:59136
	v_mov_b32_e32 v2, 0xf780
	v_mad_u32_u24 v2, v1, s9, v2
	v_cmp_gt_u32_e64 s[6:7], s6, v0
	v_add_u32_e32 v2, v35, v2
	v_add_u32_e32 v3, 0x11880, v37
	s_waitcnt vmcnt(9)
	ds_write_b128 v2, v[170:173]
	s_waitcnt vmcnt(8)
	ds_write_b128 v2, v[174:177] offset:4224
	s_waitcnt vmcnt(7)
	ds_write_b128 v3, v[178:181]
	s_waitcnt vmcnt(6)
	ds_write_b128 v2, v[182:185] offset:12672
	s_waitcnt vmcnt(5)
	ds_write_b128 v2, v[186:189] offset:16896
	s_waitcnt vmcnt(4)
	ds_write_b128 v2, v[190:193] offset:21120
	s_waitcnt vmcnt(3)
	ds_write_b128 v2, v[194:197] offset:25344
	s_and_saveexec_b64 s[24:25], s[6:7]
	s_cbranch_execz .LBB2_18
	s_waitcnt vmcnt(0)
	ds_write_b128 v2, v[220:223] offset:29568
	s_or_b64 exec, exec, s[24:25]
	s_and_saveexec_b64 s[6:7], vcc
	s_cbranch_execnz .LBB2_19

	.amdhsa_kernel _Z7k_conv4PKDF16_S0_S0_PKfS2_Pf
		.amdhsa_group_segment_fixed_size 107712
		.amdhsa_private_segment_fixed_size 0
		.amdhsa_kernarg_size 48
		.amdhsa_user_sgpr_count 2
		.amdhsa_user_sgpr_dispatch_ptr 0
		.amdhsa_user_sgpr_queue_ptr 0
		.amdhsa_user_sgpr_kernarg_segment_ptr 1
		.amdhsa_user_sgpr_dispatch_id 0
		.amdhsa_user_sgpr_kernarg_preload_length 0
		.amdhsa_user_sgpr_kernarg_preload_offset 0
		.amdhsa_user_sgpr_private_segment_size 0
		.amdhsa_uses_dynamic_stack 0
		.amdhsa_enable_private_segment 0
		.amdhsa_system_sgpr_workgroup_id_x 1
		.amdhsa_system_sgpr_workgroup_id_y 1
		.amdhsa_system_sgpr_workgroup_id_z 0
		.amdhsa_system_sgpr_workgroup_info 0
		.amdhsa_system_vgpr_workitem_id 0
		.amdhsa_next_free_vgpr 336
		.amdhsa_next_free_sgpr 96
		.amdhsa_accum_offset 224
		.amdhsa_reserve_vcc 1
		.amdhsa_float_round_mode_32 0
		.amdhsa_float_round_mode_16_64 0
		.amdhsa_float_denorm_mode_32 3
		.amdhsa_float_denorm_mode_16_64 3
		.amdhsa_dx10_clamp 1
		.amdhsa_ieee_mode 1
		.amdhsa_fp16_overflow 0
		.amdhsa_tg_split 0
		.amdhsa_exception_fp_ieee_invalid_op 0
		.amdhsa_exception_fp_denorm_src 0
		.amdhsa_exception_fp_ieee_div_zero 0
		.amdhsa_exception_fp_ieee_overflow 0
		.amdhsa_exception_fp_ieee_underflow 0
		.amdhsa_exception_fp_ieee_inexact 0
		.amdhsa_exception_int_div_zero 0
	.end_amdhsa_kernel

amdhsa.kernels:
  - .agpr_count:     0
    .args:
      - .actual_access:  read_only
        .address_space:  global
        .offset:         0
        .size:           8
        .value_kind:     global_buffer
      - .actual_access:  read_only
        .address_space:  global
        .offset:         8
        .size:           8
        .value_kind:     global_buffer
      - .actual_access:  read_only
        .address_space:  global
        .offset:         16
        .size:           8
        .value_kind:     global_buffer
      - .actual_access:  read_only
        .address_space:  global
        .offset:         24
        .size:           8
        .value_kind:     global_buffer
      - .actual_access:  read_only
        .address_space:  global
        .offset:         32
        .size:           8
        .value_kind:     global_buffer
      - .actual_access:  read_only
        .address_space:  global
        .offset:         40
        .size:           8
        .value_kind:     global_buffer
      - .actual_access:  read_only
        .address_space:  global
        .offset:         48
        .size:           8
        .value_kind:     global_buffer
      - .actual_access:  read_only
        .address_space:  global
        .offset:         56
        .size:           8
        .value_kind:     global_buffer
      - .actual_access:  write_only
        .address_space:  global
        .offset:         64
        .size:           8
        .value_kind:     global_buffer
      - .actual_access:  write_only
        .address_space:  global
        .offset:         72
        .size:           8
        .value_kind:     global_buffer
      - .actual_access:  write_only
        .address_space:  global
        .offset:         80
        .size:           8
        .value_kind:     global_buffer
      - .actual_access:  write_only
        .address_space:  global
        .offset:         88
        .size:           8
        .value_kind:     global_buffer
    .group_segment_fixed_size: 0
    .kernarg_segment_align: 8
    .kernarg_segment_size: 96
    .language:       OpenCL C
    .language_version:
      - 2
      - 0
    .max_flat_workgroup_size: 256
    .name:           _Z8k_prep_wPKfS0_S0_S0_S0_S0_S0_S0_PDF16_PfS1_S1_
    .private_segment_fixed_size: 0
    .sgpr_count:     23
    .sgpr_spill_count: 0
    .symbol:         _Z8k_prep_wPKfS0_S0_S0_S0_S0_S0_S0_PDF16_PfS1_S1_.kd
    .uniform_work_group_size: 1
    .uses_dynamic_stack: false
    .vgpr_count:     15
    .vgpr_spill_count: 0
    .wavefront_size: 64
  - .agpr_count:     0
    .args:
      - .actual_access:  read_only
        .address_space:  global
        .offset:         0
        .size:           8
        .value_kind:     global_buffer
      - .actual_access:  read_only
        .address_space:  global
        .offset:         8
        .size:           8
        .value_kind:     global_buffer
      - .actual_access:  read_only
        .address_space:  global
        .offset:         16
        .size:           8
        .value_kind:     global_buffer
      - .actual_access:  read_only
        .address_space:  global
        .offset:         24
        .size:           8
        .value_kind:     global_buffer
      - .actual_access:  write_only
        .address_space:  global
        .offset:         32
        .size:           8
        .value_kind:     global_buffer
      - .actual_access:  read_only
        .address_space:  global
        .offset:         40
        .size:           8
        .value_kind:     global_buffer
      - .actual_access:  read_only
        .address_space:  global
        .offset:         48
        .size:           8
        .value_kind:     global_buffer
      - .actual_access:  write_only
        .address_space:  global
        .offset:         56
        .size:           8
        .value_kind:     global_buffer
      - .offset:         64
        .size:           4
        .value_kind:     by_value
      - .offset:         68
        .size:           4
        .value_kind:     by_value
    .group_segment_fixed_size: 115712
    .kernarg_segment_align: 8
    .kernarg_segment_size: 72
    .language:       OpenCL C
    .language_version:
      - 2
      - 0
    .max_flat_workgroup_size: 512
    .name:           _Z8k_stageAPKfS0_S0_S0_PDF16_PKDF16_S0_S1_ii
    .private_segment_fixed_size: 0
    .sgpr_count:     28
    .sgpr_spill_count: 0
    .symbol:         _Z8k_stageAPKfS0_S0_S0_PDF16_PKDF16_S0_S1_ii.kd
    .uniform_work_group_size: 1
    .uses_dynamic_stack: false
    .vgpr_count:     251
    .vgpr_spill_count: 0
    .wavefront_size: 64
  - .agpr_count:     112
    .args:
      - .actual_access:  read_only
        .address_space:  global
        .offset:         0
        .size:           8
        .value_kind:     global_buffer
      - .actual_access:  read_only
        .address_space:  global
        .offset:         8
        .size:           8
        .value_kind:     global_buffer
      - .actual_access:  read_only
        .address_space:  global
        .offset:         16
        .size:           8
        .value_kind:     global_buffer
      - .actual_access:  read_only
        .address_space:  global
        .offset:         24
        .size:           8
        .value_kind:     global_buffer
      - .actual_access:  read_only
        .address_space:  global
        .offset:         32
        .size:           8
        .value_kind:     global_buffer
      - .actual_access:  write_only
        .address_space:  global
        .offset:         40
        .size:           8
        .value_kind:     global_buffer
    .group_segment_fixed_size: 107712
    .kernarg_segment_align: 8
    .kernarg_segment_size: 48
    .language:       OpenCL C
    .language_version:
      - 2
      - 0
    .max_flat_workgroup_size: 256
    .name:           _Z7k_conv4PKDF16_S0_S0_PKfS2_Pf
    .private_segment_fixed_size: 0
    .sgpr_count:     36
    .sgpr_spill_count: 0
    .symbol:         _Z7k_conv4PKDF16_S0_S0_PKfS2_Pf.kd
    .uniform_work_group_size: 1
    .uses_dynamic_stack: false
    .vgpr_count:     336
    .vgpr_spill_count: 0
    .wavefront_size: 64
  - .agpr_count:     0
    .args:
      - .offset:         0
        .size:           112
        .value_kind:     by_value
      - .actual_access:  read_only
        .address_space:  global
        .offset:         112
        .size:           8
        .value_kind:     global_buffer
      - .actual_access:  read_only
        .address_space:  global
        .offset:         120
        .size:           8
        .value_kind:     global_buffer
      - .actual_access:  write_only
        .address_space:  global
        .offset:         128
        .size:           8
        .value_kind:     global_buffer
      - .offset:         136
        .size:           4
        .value_kind:     by_value
      - .offset:         140
        .size:           4
        .value_kind:     by_value
      - .offset:         144
        .size:           4
        .value_kind:     by_value
    .group_segment_fixed_size: 115712
    .kernarg_segment_align: 8
    .kernarg_segment_size: 148
    .language:       OpenCL C
    .language_version:
      - 2
      - 0
    .max_flat_workgroup_size: 512
    .name:           _Z7k_stageILi0ELi8EEv8AttnArgsPKDF16_PKfPDF16_iii
    .private_segment_fixed_size: 0
    .sgpr_count:     41
    .sgpr_spill_count: 0
    .symbol:         _Z7k_stageILi0ELi8EEv8AttnArgsPKDF16_PKfPDF16_iii.kd
    .uniform_work_group_size: 1
    .uses_dynamic_stack: false
    .vgpr_count:     255
    .vgpr_spill_count: 0
    .wavefront_size: 64
  - .agpr_count:     0
    .args:
      - .offset:         0
        .size:           112
        .value_kind:     by_value
      - .actual_access:  read_only
        .address_space:  global
        .offset:         112
        .size:           8
        .value_kind:     global_buffer
      - .actual_access:  read_only
        .address_space:  global
        .offset:         120
        .size:           8
        .value_kind:     global_buffer
      - .actual_access:  write_only
        .address_space:  global
        .offset:         128
        .size:           8
        .value_kind:     global_buffer
      - .offset:         136
        .size:           4
        .value_kind:     by_value
      - .offset:         140
        .size:           4
        .value_kind:     by_value
      - .offset:         144
        .size:           4
        .value_kind:     by_value
    .group_segment_fixed_size: 82944
    .kernarg_segment_align: 8
    .kernarg_segment_size: 148
    .language:       OpenCL C
    .language_version:
      - 2
      - 0
    .max_flat_workgroup_size: 512
    .name:           _Z7k_stageILi1ELi4EEv8AttnArgsPKDF16_PKfPDF16_iii
    .private_segment_fixed_size: 0
    .sgpr_count:     55
    .sgpr_spill_count: 0
    .symbol:         _Z7k_stageILi1ELi4EEv8AttnArgsPKDF16_PKfPDF16_iii.kd
    .uniform_work_group_size: 1
    .uses_dynamic_stack: false
    .vgpr_count:     252
    .vgpr_spill_count: 0
    .wavefront_size: 64
  - .agpr_count:     0
    .args:
      - .offset:         0
        .size:           112
        .value_kind:     by_value
      - .actual_access:  read_only
        .address_space:  global
        .offset:         112
        .size:           8
        .value_kind:     global_buffer
      - .actual_access:  read_only
        .address_space:  global
        .offset:         120
        .size:           8
        .value_kind:     global_buffer
      - .actual_access:  write_only
        .address_space:  global
        .offset:         128
        .size:           8
        .value_kind:     global_buffer
      - .offset:         136
        .size:           4
        .value_kind:     by_value
      - .offset:         140
        .size:           4
        .value_kind:     by_value
      - .offset:         144
        .size:           4
        .value_kind:     by_value
    .group_segment_fixed_size: 82944
    .kernarg_segment_align: 8
    .kernarg_segment_size: 148
    .language:       OpenCL C
    .language_version:
      - 2
      - 0
    .max_flat_workgroup_size: 512
    .name:           _Z7k_stageILi0ELi4EEv8AttnArgsPKDF16_PKfPDF16_iii
    .private_segment_fixed_size: 0
    .sgpr_count:     38
    .sgpr_spill_count: 0
    .symbol:         _Z7k_stageILi0ELi4EEv8AttnArgsPKDF16_PKfPDF16_iii.kd
    .uniform_work_group_size: 1
    .uses_dynamic_stack: false
    .vgpr_count:     246
    .vgpr_spill_count: 0
    .wavefront_size: 64
  - .agpr_count:     0
    .args:
      - .offset:         0
        .size:           112
        .value_kind:     by_value
    .group_segment_fixed_size: 0
    .kernarg_segment_align: 8
    .kernarg_segment_size: 112
    .language:       OpenCL C
    .language_version:
      - 2
      - 0
    .max_flat_workgroup_size: 512
    .name:           _Z7k_attn2ILi2EEv8AttnArgs
    .private_segment_fixed_size: 0
    .sgpr_count:     102
    .sgpr_spill_count: 0
    .symbol:         _Z7k_attn2ILi2EEv8AttnArgs.kd
    .uniform_work_group_size: 1
    .uses_dynamic_stack: false
    .vgpr_count:     252
    .vgpr_spill_count: 0
    .wavefront_size: 64
